# xbf loop XN stores with sc1 (write-through) as well
# speedup vs baseline: 1.0082x; 1.0007x over previous
.LBB0_53:
	s_waitcnt lgkmcnt(0)
	global_load_dwordx4 v[16:19], v[6:7], off offset:-2048 nt
	global_load_dwordx4 v[20:23], v[6:7], off offset:-1024 nt
	global_load_dwordx4 v[24:27], v[6:7], off nt
	global_load_dwordx4 v[28:31], v[6:7], off offset:1024 nt
	v_lshl_add_u64 v[32:33], s[12:13], 0, v[2:3]
	v_add_co_u32_e32 v32, vcc, s15, v32
	s_waitcnt vmcnt(3)
	v_mul_f32_e32 v15, v17, v17
	s_waitcnt vmcnt(2)
	v_mul_f32_e32 v34, v21, v21
	s_waitcnt vmcnt(1)
	v_mul_f32_e32 v35, v25, v25
	v_fmac_f32_e32 v34, v20, v20
	v_fmac_f32_e32 v15, v16, v16
	s_waitcnt vmcnt(0)
	v_mul_f32_e32 v36, v29, v29
	v_fmac_f32_e32 v35, v24, v24
	v_fmac_f32_e32 v34, v22, v22
	v_fmac_f32_e32 v15, v18, v18
	v_bfe_u32 v37, v16, 16, 1
	v_bfe_u32 v38, v17, 16, 1
	v_bfe_u32 v39, v18, 16, 1
	v_fmac_f32_e32 v36, v28, v28
	v_fmac_f32_e32 v35, v26, v26
	v_fmac_f32_e32 v34, v23, v23
	v_fmac_f32_e32 v15, v19, v19
	v_bfe_u32 v40, v19, 16, 1
	v_bfe_u32 v41, v20, 16, 1
	v_bfe_u32 v43, v22, 16, 1
	v_add3_u32 v37, v16, v37, s2
	v_add3_u32 v17, v17, v38, s2
	v_add3_u32 v38, v18, v39, s2
	v_fmac_f32_e32 v36, v30, v30
	v_fmac_f32_e32 v35, v27, v27
	v_add_f32_e32 v15, v15, v34
	v_bfe_u32 v42, v21, 16, 1
	v_bfe_u32 v44, v23, 16, 1
	v_add3_u32 v39, v19, v40, s2
	v_add3_u32 v20, v20, v41, s2
	v_add3_u32 v40, v22, v43, s2
	v_lshrrev_b32_e32 v16, 16, v37
	v_lshrrev_b32_e32 v22, 16, v38
	v_fmac_f32_e32 v36, v31, v31
	v_add_f32_e32 v15, v15, v35
	v_addc_co_u32_e32 v33, vcc, 0, v33, vcc
	v_add3_u32 v21, v21, v42, s2
	v_add3_u32 v41, v23, v44, s2
	v_lshrrev_b32_e32 v20, 16, v20
	v_lshrrev_b32_e32 v37, 16, v40
	v_and_or_b32 v16, v17, s3, v16
	v_and_or_b32 v17, v39, s3, v22
	v_add_f32_e32 v15, v15, v36
	v_and_or_b32 v20, v21, s3, v20
	v_and_or_b32 v21, v41, s3, v37
	global_store_dwordx2 v[32:33], v[16:17], off sc1
	global_store_dwordx2 v[32:33], v[20:21], off offset:512 sc1
	ds_bpermute_b32 v17, v8, v15
	v_bfe_u32 v45, v24, 16, 1
	v_add3_u32 v24, v24, v45, s2
	v_bfe_u32 v18, v25, 16, 1
	v_lshrrev_b32_e32 v16, 16, v24
	s_waitcnt lgkmcnt(0)
	v_add_f32_e32 v15, v15, v17
	ds_bpermute_b32 v17, v9, v15
	v_add3_u32 v18, v25, v18, s2
	v_and_or_b32 v16, v18, s3, v16
	v_bfe_u32 v18, v26, 16, 1
	v_add3_u32 v18, v26, v18, s2
	s_waitcnt lgkmcnt(0)
	v_add_f32_e32 v15, v15, v17
	ds_bpermute_b32 v20, v10, v15
	v_bfe_u32 v19, v27, 16, 1
	v_lshrrev_b32_e32 v18, 16, v18
	v_add3_u32 v17, v27, v19, s2
	v_and_or_b32 v17, v17, s3, v18
	s_waitcnt lgkmcnt(0)
	v_add_f32_e32 v15, v15, v20
	global_store_dwordx2 v[32:33], v[16:17], off offset:1024 sc1
	ds_bpermute_b32 v17, v11, v15
	v_bfe_u32 v16, v28, 16, 1
	v_add3_u32 v16, v28, v16, s2
	v_bfe_u32 v18, v29, 16, 1
	v_lshrrev_b32_e32 v16, 16, v16
	s_waitcnt lgkmcnt(0)
	v_add_f32_e32 v15, v15, v17
	ds_bpermute_b32 v17, v12, v15
	v_add3_u32 v18, v29, v18, s2
	v_and_or_b32 v18, v18, s3, v16
	v_bfe_u32 v16, v30, 16, 1
	v_add3_u32 v16, v30, v16, s2
	s_waitcnt lgkmcnt(0)
	v_add_f32_e32 v15, v15, v17
	v_lshrrev_b32_e32 v19, 16, v16
	ds_bpermute_b32 v16, v13, v15
	v_bfe_u32 v17, v31, 16, 1
	v_add3_u32 v17, v31, v17, s2
	v_and_or_b32 v19, v17, s3, v19
	global_store_dwordx2 v[32:33], v[18:19], off offset:1536 sc1
	s_and_saveexec_b64 s[18:19], s[4:5]
	s_cbranch_execz .LBB0_52
	s_waitcnt lgkmcnt(0)
	v_add_f32_e32 v15, v15, v16
	v_fmamk_f32 v15, v15, 0x3a800000, v4
	v_mul_f32_e32 v16, 0x4f800000, v15
	v_cmp_gt_f32_e32 vcc, s20, v15
	s_nop 1
	v_cndmask_b32_e32 v15, v15, v16, vcc
	v_sqrt_f32_e32 v16, v15
	s_nop 0
	v_add_u32_e32 v17, -1, v16
	v_fma_f32 v19, -v17, v16, v15
	v_add_u32_e32 v18, 1, v16
	v_cmp_ge_f32_e64 s[6:7], 0, v19
	s_nop 1
	v_cndmask_b32_e64 v17, v16, v17, s[6:7]
	v_fma_f32 v16, -v18, v16, v15
	v_cmp_lt_f32_e64 s[6:7], 0, v16
	s_nop 1
	v_cndmask_b32_e64 v16, v17, v18, s[6:7]
	v_mul_f32_e32 v17, 0x37800000, v16
	v_cndmask_b32_e32 v16, v16, v17, vcc
	v_cmp_class_f32_e32 vcc, v15, v14
	s_nop 1
	v_cndmask_b32_e32 v15, v16, v15, vcc
	v_div_scale_f32 v16, s[6:7], v15, v15, 1.0
	v_rcp_f32_e32 v17, v16
	s_add_u32 s6, s12, s0
	s_addc_u32 s7, s13, s1
	v_fma_f32 v18, -v16, v17, 1.0
	v_fmac_f32_e32 v17, v18, v17
	v_div_scale_f32 v18, vcc, 1.0, v15, 1.0
	v_mul_f32_e32 v19, v18, v17
	v_fma_f32 v20, -v16, v19, v18
	v_fmac_f32_e32 v19, v20, v17
	v_fma_f32 v16, -v16, v19, v18
	v_div_fmas_f32 v16, v16, v17, v19
	v_div_fixup_f32 v15, v16, v15, 1.0
	global_store_dword v5, v15, s[6:7]
	s_branch .LBB0_52
